# main: x loads before A loads with counted waits, halo LDS-DMA issued before first barrier
# speedup vs baseline: 1.0052x; 1.0052x over previous
_Z7na_mainPKDF16_PKhS0_PKfS4_S4_S4_Pf:
	s_lshl_b32 s3, s2, 5
	s_and_b32 s3, s3, 0xe0
	s_ashr_i32 s2, s2, 3
	s_add_i32 s3, s3, s2
	s_ashr_i32 s2, s3, 6
	s_lshl_b32 s3, s3, 5
	s_and_b32 s14, s3, 0x7e0
	v_mov_b32_e32 v1, 0x7c0
	s_load_dwordx8 s[4:11], s[0:1], 0x0
	v_med3_u32 v1, s14, 32, v1
	v_subrev_u32_e32 v97, 32, v1
	s_ashr_i32 s3, s2, 31
	v_lshlrev_b32_e32 v58, 1, v97
	s_lshl_b64 s[12:13], s[2:3], 12
	v_mov_b32_e32 v59, 0
	v_sub_u32_e32 v60, s14, v97
	v_lshl_add_u64 v[10:11], s[12:13], 0, v[58:59]
	v_lshlrev_b64 v[2:3], 9, v[10:11]
	v_lshl_or_b32 v22, v60, 6, v0
	s_waitcnt lgkmcnt(0)
	v_lshl_add_u64 v[20:21], s[4:5], 0, v[2:3]
	v_ashrrev_i32_e32 v23, 31, v22
	v_lshl_add_u64 v[2:3], v[22:23], 4, v[20:21]
	global_load_dwordx4 v[12:15], v[2:3], off
	v_or_b32_e32 v28, 0x200, v22
	v_ashrrev_i32_e32 v29, 31, v28
	v_lshl_add_u64 v[2:3], v[28:29], 4, v[20:21]
	global_load_dwordx4 v[16:19], v[2:3], off
	v_or_b32_e32 v184, 0x400, v22
	v_ashrrev_i32_e32 v185, 31, v184
	v_lshl_add_u64 v[184:185], v[184:185], 4, v[20:21]
	v_or_b32_e32 v188, 0x600, v22
	v_ashrrev_i32_e32 v189, 31, v188
	v_lshl_add_u64 v[188:189], v[188:189], 4, v[20:21]
	global_load_dwordx4 v[184:187], v[184:185], off
	global_load_dwordx4 v[188:191], v[188:189], off
	v_lshrrev_b32_e32 v99, 6, v0
	v_and_b32_e32 v98, 63, v0
	v_lshlrev_b32_e32 v118, 13, v99
	v_lshl_or_b32 v58, v98, 5, v118
	s_movk_i32 s15, 0x1000
	v_lshl_add_u64 v[24:25], s[6:7], 0, v[58:59]
	v_or_b32_e32 v32, 0x400, v22
	v_or_b32_e32 v62, 0x600, v22
	v_add_co_u32_e32 v64, vcc, s15, v24
	s_mov_b64 s[12:13], 0x1000
	s_mov_b64 s[16:17], 0x1800
	v_lshlrev_b32_e32 v72, 1, v60
	v_lshrrev_b32_e32 v23, 5, v22
	v_and_b32_e32 v34, 32, v22
	v_ashrrev_i32_e32 v33, 31, v32
	v_ashrrev_i32_e32 v63, 31, v62
	v_addc_co_u32_e32 v65, vcc, 0, v25, vcc
	global_load_dwordx4 v[6:9], v58, s[6:7] offset:16
	global_load_dwordx4 v[2:5], v58, s[6:7]
	global_load_dwordx4 v[54:57], v58, s[6:7] offset:2064
	global_load_dwordx4 v[50:53], v58, s[6:7] offset:2048
	v_lshrrev_b32_e32 v58, 6, v22
	v_bfe_u32 v73, v22, 8, 2
	v_lshl_add_u64 v[26:27], v[24:25], 0, s[12:13]
	v_lshl_add_u64 v[24:25], v[24:25], 0, s[16:17]
	v_cmp_ne_u32_e32 vcc, 0, v34
	v_sub_u32_e32 v75, v23, v72
	global_load_dwordx4 v[42:45], v[64:65], off
	global_load_dwordx4 v[46:49], v[26:27], off offset:16
	global_load_dwordx4 v[34:37], v[64:65], off offset:2048
	global_load_dwordx4 v[38:41], v[24:25], off offset:16
	v_mov_b32_e32 v61, 0x60
	v_cndmask_b32_e32 v74, 0, v61, vcc
	v_add_u32_e32 v33, v74, v58
	v_lshlrev_b32_e32 v64, 2, v33
	v_bfe_u32 v96, v0, 4, 1
	v_and_b32_e32 v100, 15, v0
	v_mov_b32_e32 v30, v59
	v_mov_b32_e32 v31, v59
	v_and_b32_e32 v64, 12, v64
	v_mul_u32_u24_e32 v29, 0xc000, v96
	v_bitop3_b32 v64, v64, v100, v73 bitop3:0x36
	v_lshl_or_b32 v64, v64, 4, v29
	v_lshlrev_b32_e32 v63, 1, v75
	v_lshl_add_u32 v33, v33, 8, v64
	v_bfe_u32 v71, v0, 1, 4
	v_and_b32_e32 v70, 32, v0
	v_lshlrev_b32_e32 v1, 3, v0
	v_lshrrev_b32_e32 v58, 1, v75
	v_and_b32_e32 v1, 8, v1
	v_add_lshl_u32 v58, v58, v70, 8
	v_lshlrev_b32_e32 v121, 3, v99
	v_bfe_u32 v101, v0, 4, 2
	v_lshlrev_b32_e32 v102, 2, v101
	v_and_b32_e32 v116, 31, v0
	v_bfe_u32 v119, v0, 5, 1
	v_lshlrev_b32_e32 v124, 1, v119
	v_lshlrev_b32_e32 v117, 8, v116
	v_lshrrev_b32_e32 v95, 4, v0
	s_movk_i32 s16, 0x60
	s_mov_b32 s17, 0xc000
	s_waitcnt vmcnt(11)
	v_cvt_f32_f16_e32 v65, v12
	v_cvt_f32_f16_sdwa v66, v12 dst_sel:DWORD dst_unused:UNUSED_PAD src0_sel:WORD_1
	v_cvt_f32_f16_e32 v69, v14
	v_cvt_f32_f16_sdwa v74, v14 dst_sel:DWORD dst_unused:UNUSED_PAD src0_sel:WORD_1
	v_cvt_f32_f16_e32 v67, v13
	v_cvt_f32_f16_sdwa v68, v13 dst_sel:DWORD dst_unused:UNUSED_PAD src0_sel:WORD_1
	v_cvt_f32_f16_e32 v76, v15
	v_cvt_f32_f16_sdwa v77, v15 dst_sel:DWORD dst_unused:UNUSED_PAD src0_sel:WORD_1
	v_cvt_pk_fp8_f32 v30, v65, v66
	v_cvt_pk_fp8_f32 v31, v69, v74
	ds_write_b128 v33, v[12:15]
	v_and_b32_e32 v12, 12, v63
	v_bfe_u32 v13, v75, 3, 2
	v_cvt_pk_fp8_f32 v30, v67, v68 op_sel:[0,0,1]
	v_cvt_pk_fp8_f32 v31, v76, v77 op_sel:[0,0,1]
	v_bitop3_b32 v12, v12, v71, v13 bitop3:0x36
	v_lshlrev_b32_e32 v12, 4, v12
	v_or3_b32 v12, v58, v12, v1
	v_add_u32_e32 v12, 0x23800, v12
	ds_write_b64 v12, v[30:31]
	v_and_b32_e32 v12, 32, v28
	v_cmp_ne_u32_e32 vcc, 0, v12
	v_lshrrev_b32_e32 v13, 6, v28
	v_bfe_u32 v15, v28, 8, 2
	v_cndmask_b32_e32 v12, 0, v61, vcc
	v_add_u32_e32 v12, v12, v13
	v_lshlrev_b32_e32 v13, 2, v12
	v_and_b32_e32 v13, 12, v13
	v_bitop3_b32 v13, v13, v100, v15 bitop3:0x36
	v_lshl_or_b32 v13, v13, 4, v29
	v_lshl_add_u32 v12, v12, 8, v13
	s_waitcnt vmcnt(10)
	v_cvt_f32_f16_e32 v13, v16
	v_cvt_f32_f16_sdwa v15, v16 dst_sel:DWORD dst_unused:UNUSED_PAD src0_sel:WORD_1
	ds_write_b128 v12, v[16:19]
	v_mov_b32_e32 v12, v59
	v_cvt_f32_f16_e32 v16, v17
	v_cvt_pk_fp8_f32 v12, v13, v15
	v_cvt_f32_f16_e32 v15, v18
	v_cvt_f32_f16_sdwa v18, v18 dst_sel:DWORD dst_unused:UNUSED_PAD src0_sel:WORD_1
	v_cvt_f32_f16_sdwa v17, v17 dst_sel:DWORD dst_unused:UNUSED_PAD src0_sel:WORD_1
	v_mov_b32_e32 v13, v59
	v_lshrrev_b32_e32 v14, 5, v28
	v_cvt_f32_f16_e32 v28, v19
	v_cvt_f32_f16_sdwa v19, v19 dst_sel:DWORD dst_unused:UNUSED_PAD src0_sel:WORD_1
	v_cvt_pk_fp8_f32 v13, v15, v18
	v_sub_u32_e32 v14, v14, v72
	v_cvt_pk_fp8_f32 v12, v16, v17 op_sel:[0,0,1]
	v_lshlrev_b32_e32 v16, 1, v14
	v_lshrrev_b32_e32 v15, 1, v14
	v_and_b32_e32 v16, 12, v16
	v_bfe_u32 v14, v14, 3, 2
	v_cvt_pk_fp8_f32 v13, v28, v19 op_sel:[0,0,1]
	v_bitop3_b32 v14, v16, v71, v14 bitop3:0x36
	v_add_lshl_u32 v15, v15, v70, 8
	v_lshlrev_b32_e32 v14, 4, v14
	v_or3_b32 v14, v15, v14, v1
	v_add_u32_e32 v14, 0x23800, v14
	ds_write_b64 v14, v[12:13]
	v_and_b32_e32 v12, 32, v32
	v_cmp_ne_u32_e32 vcc, 0, v12
	v_lshrrev_b32_e32 v13, 6, v32
	s_waitcnt vmcnt(9)
	v_cvt_f32_f16_sdwa v15, v184 dst_sel:DWORD dst_unused:UNUSED_PAD src0_sel:WORD_1
	v_cndmask_b32_e32 v12, 0, v61, vcc
	v_add_u32_e32 v12, v12, v13
	v_lshlrev_b32_e32 v13, 2, v12
	v_and_b32_e32 v13, 12, v13
	v_bitop3_b32 v13, v13, v100, v73 bitop3:0x36
	v_lshl_or_b32 v13, v13, 4, v29
	v_lshl_add_u32 v12, v12, 8, v13
	v_cvt_f32_f16_e32 v13, v184
	ds_write_b128 v12, v[184:187]
	v_mov_b32_e32 v12, v59
	v_cvt_f32_f16_sdwa v18, v186 dst_sel:DWORD dst_unused:UNUSED_PAD src0_sel:WORD_1
	v_cvt_pk_fp8_f32 v12, v13, v15
	v_cvt_f32_f16_e32 v15, v186
	v_cvt_f32_f16_e32 v16, v185
	v_cvt_f32_f16_sdwa v17, v185 dst_sel:DWORD dst_unused:UNUSED_PAD src0_sel:WORD_1
	v_mov_b32_e32 v13, v59
	v_lshrrev_b32_e32 v14, 5, v32
	v_cvt_f32_f16_e32 v19, v187
	v_cvt_f32_f16_sdwa v20, v187 dst_sel:DWORD dst_unused:UNUSED_PAD src0_sel:WORD_1
	v_cvt_pk_fp8_f32 v13, v15, v18
	v_sub_u32_e32 v14, v14, v72
	v_cvt_pk_fp8_f32 v12, v16, v17 op_sel:[0,0,1]
	v_lshlrev_b32_e32 v16, 1, v14
	v_lshrrev_b32_e32 v15, 1, v14
	v_and_b32_e32 v16, 12, v16
	v_bfe_u32 v14, v14, 3, 2
	v_cvt_pk_fp8_f32 v13, v19, v20 op_sel:[0,0,1]
	v_bitop3_b32 v14, v16, v71, v14 bitop3:0x36
	v_add_lshl_u32 v15, v15, v70, 8
	v_lshlrev_b32_e32 v14, 4, v14
	v_or3_b32 v14, v15, v14, v1
	v_add_u32_e32 v14, 0x23800, v14
	ds_write_b64 v14, v[12:13]
	v_and_b32_e32 v12, 32, v62
	v_cmp_ne_u32_e32 vcc, 0, v12
	v_lshrrev_b32_e32 v13, 6, v62
	v_bfe_u32 v15, v62, 8, 2
	v_cndmask_b32_e32 v12, 0, v61, vcc
	v_add_u32_e32 v12, v12, v13
	v_lshlrev_b32_e32 v13, 2, v12
	v_and_b32_e32 v13, 12, v13
	v_bitop3_b32 v13, v13, v100, v15 bitop3:0x36
	v_lshl_or_b32 v13, v13, 4, v29
	v_lshl_add_u32 v12, v12, 8, v13
	s_waitcnt vmcnt(8)
	v_cvt_f32_f16_e32 v13, v188
	v_cvt_f32_f16_sdwa v15, v188 dst_sel:DWORD dst_unused:UNUSED_PAD src0_sel:WORD_1
	ds_write_b128 v12, v[188:191]
	v_mov_b32_e32 v12, v59
	v_cvt_f32_f16_sdwa v18, v190 dst_sel:DWORD dst_unused:UNUSED_PAD src0_sel:WORD_1
	v_cvt_pk_fp8_f32 v12, v13, v15
	v_cvt_f32_f16_e32 v15, v190
	v_cvt_f32_f16_e32 v16, v189
	v_cvt_f32_f16_sdwa v17, v189 dst_sel:DWORD dst_unused:UNUSED_PAD src0_sel:WORD_1
	v_mov_b32_e32 v13, v59
	v_lshrrev_b32_e32 v14, 5, v62
	v_cvt_f32_f16_e32 v19, v191
	v_cvt_f32_f16_sdwa v20, v191 dst_sel:DWORD dst_unused:UNUSED_PAD src0_sel:WORD_1
	v_cvt_pk_fp8_f32 v13, v15, v18
	v_sub_u32_e32 v14, v14, v72
	v_cvt_pk_fp8_f32 v12, v16, v17 op_sel:[0,0,1]
	v_lshlrev_b32_e32 v16, 1, v14
	v_lshrrev_b32_e32 v15, 1, v14
	v_and_b32_e32 v16, 12, v16
	v_bfe_u32 v14, v14, 3, 2
	v_cvt_pk_fp8_f32 v13, v19, v20 op_sel:[0,0,1]
	v_bitop3_b32 v14, v16, v71, v14 bitop3:0x36
	v_add_lshl_u32 v15, v15, v70, 8
	v_lshlrev_b32_e32 v14, 4, v14
	v_or3_b32 v14, v15, v14, v1
	v_add_u32_e32 v14, 0x23800, v14
	v_cmp_lt_i32_e32 vcc, v121, v60
	ds_write_b64 v14, v[12:13]
	v_mov_b32_e32 v15, v59
	v_cndmask_b32_e64 v12, 32, 0, vcc
	v_add_u32_e32 v16, v12, v121
	v_or_b32_e32 v12, v16, v101
	v_lshlrev_b32_e32 v58, 1, v12
	v_lshrrev_b32_e32 v12, 5, v0
	v_and_b32_e32 v12, 2, v12
	v_bitop3_b32 v14, v102, v100, v12 bitop3:0x36
	v_lshl_add_u64 v[12:13], v[10:11], 0, v[58:59]
	v_lshlrev_b64 v[12:13], 9, v[12:13]
	v_lshlrev_b32_e32 v16, 8, v16
	v_lshl_add_u64 v[12:13], s[4:5], 0, v[12:13]
	v_lshlrev_b32_e32 v14, 4, v14
	v_readfirstlane_b32 s6, v16
	v_add_u32_e32 v17, 0xc000, v16
	v_lshl_add_u64 v[12:13], v[12:13], 0, v[14:15]
	s_mov_b32 m0, s6
	s_mov_b64 s[6:7], 0x100
	v_readfirstlane_b32 s12, v17
	global_load_lds_dwordx4 v[12:13], off
	v_lshl_add_u64 v[12:13], v[12:13], 0, s[6:7]
	s_mov_b32 m0, s12
	v_or_b32_e32 v58, 1, v58
	global_load_lds_dwordx4 v[12:13], off
	v_lshl_add_u64 v[12:13], v[10:11], 0, v[58:59]
	v_lshlrev_b64 v[12:13], 9, v[12:13]
	v_lshl_add_u64 v[12:13], s[4:5], 0, v[12:13]
	v_lshl_add_u64 v[12:13], v[12:13], 0, v[14:15]
	v_add_u32_e32 v14, 0x6000, v16
	v_bfe_u32 v61, v0, 2, 2
	v_readfirstlane_b32 s12, v14
	v_add_u32_e32 v14, 0x12000, v16
	s_mov_b32 m0, s12
	v_readfirstlane_b32 s12, v14
	global_load_lds_dwordx4 v[12:13], off
	v_lshl_add_u64 v[12:13], v[12:13], 0, s[6:7]
	s_mov_b32 m0, s12
	v_add_u32_e32 v18, 0x23800, v117
	global_load_lds_dwordx4 v[12:13], off
	v_or_b32_e32 v12, 4, v121
	v_cmp_lt_i32_e32 vcc, v12, v60
	s_nop 1
	v_cndmask_b32_e64 v13, 32, 0, vcc
	v_add_u32_e32 v16, v13, v12
	v_or_b32_e32 v13, v16, v101
	v_lshlrev_b32_e32 v58, 1, v13
	v_bfe_u32 v12, v12, 2, 2
	v_bitop3_b32 v14, v102, v100, v12 bitop3:0x36
	v_lshl_add_u64 v[12:13], v[10:11], 0, v[58:59]
	v_lshlrev_b64 v[12:13], 9, v[12:13]
	v_lshlrev_b32_e32 v16, 8, v16
	v_lshl_add_u64 v[12:13], s[4:5], 0, v[12:13]
	v_lshlrev_b32_e32 v14, 4, v14
	v_readfirstlane_b32 s12, v16
	v_add_u32_e32 v17, 0xc000, v16
	v_lshl_add_u64 v[12:13], v[12:13], 0, v[14:15]
	s_mov_b32 m0, s12
	v_readfirstlane_b32 s12, v17
	v_or_b32_e32 v58, 1, v58
	global_load_lds_dwordx4 v[12:13], off
	v_lshl_add_u64 v[12:13], v[12:13], 0, s[6:7]
	s_mov_b32 m0, s12
	v_lshl_add_u64 v[10:11], v[10:11], 0, v[58:59]
	global_load_lds_dwordx4 v[12:13], off
	v_lshlrev_b64 v[10:11], 9, v[10:11]
	v_add_u32_e32 v12, 0x6000, v16
	v_lshl_add_u64 v[10:11], s[4:5], 0, v[10:11]
	v_readfirstlane_b32 s4, v12
	v_add_u32_e32 v12, 0x12000, v16
	v_lshl_add_u64 v[10:11], v[10:11], 0, v[14:15]
	s_mov_b32 m0, s4
	v_readfirstlane_b32 s4, v12
	global_load_lds_dwordx4 v[10:11], off
	v_lshl_add_u64 v[10:11], v[10:11], 0, s[6:7]
	s_mov_b32 m0, s4
	s_nop 0
	global_load_lds_dwordx4 v[10:11], off
	s_waitcnt lgkmcnt(0)
	s_barrier
	v_lshlrev_b32_e32 v10, 2, v0
	v_and_b32_e32 v94, 12, v10
	v_or_b32_e32 v120, v94, v61
	v_bitop3_b32 v10, v124, v94, v61 bitop3:0x1e
	v_lshl_or_b32 v14, v10, 4, v18
	v_bitop3_b32 v10, v124, v120, 1 bitop3:0x36
	v_lshl_or_b32 v19, v10, 4, v18
	s_load_dwordx4 s[4:7], s[0:1], 0x20
	s_load_dwordx2 s[12:13], s[0:1], 0x38
	ds_read_b128 v[10:13], v14
	ds_read_b128 v[62:65], v14 offset:8192
	ds_read_b128 v[14:17], v19
	ds_read_b128 v[66:69], v19 offset:8192
	v_bitop3_b32 v19, v124, v120, 4 bitop3:0x36
	v_lshl_or_b32 v19, v19, 4, v18
	v_bitop3_b32 v20, v124, v120, 5 bitop3:0x36
	v_lshl_or_b32 v20, v20, 4, v18
	ds_read_b128 v[70:73], v19
	ds_read_b128 v[78:81], v19 offset:8192
	ds_read_b128 v[74:77], v20
	ds_read_b128 v[82:85], v20 offset:8192
	v_bitop3_b32 v19, v124, v120, 8 bitop3:0x36
	v_lshl_or_b32 v19, v19, 4, v18
	v_bitop3_b32 v20, v124, v120, 9 bitop3:0x36
	v_lshl_or_b32 v20, v20, 4, v18
	ds_read_b128 v[86:89], v19
	ds_read_b128 v[104:107], v19 offset:8192
	ds_read_b128 v[90:93], v20
	ds_read_b128 v[108:111], v20 offset:8192
	v_bitop3_b32 v19, v124, v120, 12 bitop3:0x36
	v_lshl_or_b32 v19, v19, 4, v18
	v_bitop3_b32 v20, v124, v120, 13 bitop3:0x36
	v_lshl_or_b32 v18, v20, 4, v18
	ds_read_b128 v[126:129], v19
	ds_read_b128 v[134:137], v19 offset:8192
	ds_read_b128 v[130:133], v18
	ds_read_b128 v[138:141], v18 offset:8192
	v_mov_b32_e32 v103, 0x7f
	v_lshlrev_b32_e32 v58, 7, v99
	v_or_b32_e32 v122, 0x18000, v117
	s_waitcnt vmcnt(8) lgkmcnt(0)
	v_mfma_scale_f32_32x32x64_f8f6f4 v[18:33], v[2:9], v[10:17], 0, v103, v103 op_sel_hi:[0,0,0]
	v_lshlrev_b32_e32 v125, 3, v119
	v_or_b32_e32 v123, 0x1a000, v117
	v_mfma_scale_f32_32x32x64_f8f6f4 v[2:17], v[2:9], v[62:69], 0, v103, v103 op_sel_hi:[0,0,0]
	v_and_b32_e32 v62, 12, v95
	v_mfma_scale_f32_32x32x64_f8f6f4 v[18:33], v[50:57], v[70:77], v[18:33], v103, v103 op_sel_hi:[0,0,0]
	v_mfma_scale_f32_32x32x64_f8f6f4 v[2:17], v[50:57], v[78:85], v[2:17], v103, v103 op_sel_hi:[0,0,0]
	v_lshl_add_u64 v[50:51], s[10:11], 0, v[58:59]
	v_lshlrev_b32_e32 v58, 4, v119
	v_lshl_add_u64 v[54:55], v[50:51], 0, v[58:59]
	global_load_dwordx4 v[50:53], v[54:55], off
	s_brev_b32 s10, 60
	v_lshlrev_b32_e32 v58, 6, v0
	v_and_b32_e32 v58, 0x4000, v58
	v_or3_b32 v63, v122, v58, v125
	v_or3_b32 v58, v123, v58, v125
	v_mfma_scale_f32_32x32x64_f8f6f4 v[18:33], v[42:49], v[86:93], v[18:33], v103, v103 op_sel_hi:[0,0,0]
	v_mfma_scale_f32_32x32x64_f8f6f4 v[2:17], v[42:49], v[104:111], v[2:17], v103, v103 op_sel_hi:[0,0,0]
	global_load_dwordx4 v[42:45], v[54:55], off offset:32
	global_load_dwordx4 v[46:49], v[54:55], off offset:64
	s_nop 0
	global_load_dwordx4 v[54:57], v[54:55], off offset:96
	v_mfma_scale_f32_32x32x64_f8f6f4 v[2:17], v[34:41], v[134:141], v[2:17], v103, v103 op_sel_hi:[0,0,0]
	v_mfma_scale_f32_32x32x64_f8f6f4 v[18:33], v[34:41], v[126:133], v[18:33], v103, v103 op_sel_hi:[0,0,0]
	s_waitcnt vmcnt(0)
	s_nop 15
	s_nop 1
	v_fma_f32 v2, v2, s10, v50
	v_fma_f32 v3, v3, s10, v51
	v_fma_f32 v4, v4, s10, v52
	v_fma_f32 v5, v5, s10, v53
	v_cvt_pk_f16_f32 v2, v2, v3
	v_cvt_pk_f16_f32 v3, v4, v5
	v_bitop3_b32 v4, v95, v120, 12 bitop3:0x6c
	v_pk_fma_f32 v[18:19], v[18:19], s[10:11], v[50:51] op_sel_hi:[1,0,1]
	v_pk_fma_f32 v[20:21], v[20:21], s[10:11], v[52:53] op_sel_hi:[1,0,1]
	v_lshlrev_b32_e32 v4, 4, v4
	v_cvt_pk_f16_f32 v18, v18, v19
	v_cvt_pk_f16_f32 v19, v20, v21
	v_or_b32_e32 v5, v63, v4
	v_or_b32_e32 v4, v58, v4
	ds_write_b64 v5, v[18:19]
	ds_write_b64 v4, v[2:3]
	v_pk_fma_f32 v[2:3], v[22:23], s[10:11], v[42:43] op_sel_hi:[1,0,1]
	v_pk_fma_f32 v[4:5], v[6:7], s[10:11], v[42:43] op_sel_hi:[1,0,1]
	v_pk_fma_f32 v[6:7], v[24:25], s[10:11], v[44:45] op_sel_hi:[1,0,1]
	v_cvt_pk_f16_f32 v2, v2, v3
	v_cvt_pk_f16_f32 v3, v6, v7
	v_pk_fma_f32 v[6:7], v[8:9], s[10:11], v[44:45] op_sel_hi:[1,0,1]
	v_cvt_pk_f16_f32 v4, v4, v5
	v_cvt_pk_f16_f32 v5, v6, v7
	v_bitop3_b32 v6, v62, v120, 1 bitop3:0x36
	v_lshlrev_b32_e32 v6, 4, v6
	v_or_b32_e32 v7, v63, v6
	ds_write_b64 v7, v[2:3]
	v_or_b32_e32 v2, v58, v6
	ds_write_b64 v2, v[4:5]
	v_pk_fma_f32 v[2:3], v[26:27], s[10:11], v[46:47] op_sel_hi:[1,0,1]
	v_pk_fma_f32 v[6:7], v[28:29], s[10:11], v[48:49] op_sel_hi:[1,0,1]
	v_cvt_pk_f16_f32 v2, v2, v3
	v_pk_fma_f32 v[4:5], v[10:11], s[10:11], v[46:47] op_sel_hi:[1,0,1]
	v_cvt_pk_f16_f32 v3, v6, v7
	v_pk_fma_f32 v[6:7], v[12:13], s[10:11], v[48:49] op_sel_hi:[1,0,1]
	v_cvt_pk_f16_f32 v4, v4, v5
	v_cvt_pk_f16_f32 v5, v6, v7
	v_bitop3_b32 v6, v62, v120, 2 bitop3:0x36
	v_lshlrev_b32_e32 v6, 4, v6
	v_or_b32_e32 v7, v63, v6
	ds_write_b64 v7, v[2:3]
	v_or_b32_e32 v2, v58, v6
	ds_write_b64 v2, v[4:5]
	v_pk_fma_f32 v[2:3], v[30:31], s[10:11], v[54:55] op_sel_hi:[1,0,1]
	v_pk_fma_f32 v[6:7], v[32:33], s[10:11], v[56:57] op_sel_hi:[1,0,1]
	v_cvt_pk_f16_f32 v2, v2, v3
	v_pk_fma_f32 v[4:5], v[14:15], s[10:11], v[54:55] op_sel_hi:[1,0,1]
	v_cvt_pk_f16_f32 v3, v6, v7
	v_pk_fma_f32 v[6:7], v[16:17], s[10:11], v[56:57] op_sel_hi:[1,0,1]
	v_cvt_pk_f16_f32 v4, v4, v5
	v_cvt_pk_f16_f32 v5, v6, v7
	v_bitop3_b32 v6, v62, v120, 3 bitop3:0x36
	v_lshlrev_b32_e32 v6, 4, v6
	v_or_b32_e32 v7, v63, v6
	ds_write_b64 v7, v[2:3]
	v_or_b32_e32 v2, v58, v6
	ds_write_b64 v2, v[4:5]
	v_lshlrev_b32_e32 v2, 8, v101
	s_waitcnt lgkmcnt(0)
	s_barrier
	global_load_dwordx4 v[30:33], v2, s[4:5]
	global_load_dwordx4 v[34:37], v2, s[4:5] offset:16
	global_load_dwordx4 v[38:41], v2, s[4:5] offset:48
	global_load_dwordx4 v[42:45], v2, s[4:5] offset:32
	global_load_dwordx4 v[46:49], v2, s[4:5] offset:80
	global_load_dwordx4 v[50:53], v2, s[4:5] offset:64
	global_load_dwordx4 v[54:57], v2, s[4:5] offset:112
	global_load_dwordx4 v[62:65], v2, s[4:5] offset:96
	global_load_dwordx4 v[66:69], v2, s[4:5] offset:144
	global_load_dwordx4 v[70:73], v2, s[4:5] offset:128
	global_load_dwordx4 v[74:77], v2, s[4:5] offset:176
	global_load_dwordx4 v[78:81], v2, s[4:5] offset:160
	global_load_dwordx4 v[82:85], v2, s[4:5] offset:208
	global_load_dwordx4 v[86:89], v2, s[4:5] offset:192
	global_load_dwordx4 v[90:93], v2, s[4:5] offset:240
	global_load_dwordx4 v[104:107], v2, s[4:5] offset:224
	v_lshrrev_b32_e32 v27, 8, v0
	v_lshrrev_b32_e32 v3, 3, v0
	v_and_b32_e32 v3, 16, v3
	v_mul_u32_u24_e32 v28, 0x60, v27
	v_lshlrev_b32_e32 v26, 5, v27
	v_or_b32_e32 v146, v3, v100
	v_or_b32_e32 v147, v28, v100
	v_or_b32_e32 v4, v146, v26
	v_or_b32_e32 v3, v147, v3
	v_lshlrev_b32_e32 v4, 8, v4
	v_add_u32_e32 v3, v3, v60
	v_or_b32_e32 v5, 0x18000, v4
	v_bitop3_b32 v11, v101, v120, 12 bitop3:0x36
	v_or_b32_e32 v95, 0x1c000, v4
	v_lshlrev_b32_e32 v29, 3, v101
	v_lshlrev_b32_e32 v4, 8, v3
	v_lshlrev_b32_e32 v12, 2, v3
	v_bfe_u32 v3, v3, 2, 2
	v_bitop3_b32 v6, v101, v94, v61 bitop3:0x1e
	v_bitop3_b32 v8, v101, v120, 4 bitop3:0x36
	v_bitop3_b32 v10, v101, v120, 8 bitop3:0x36
	v_lshlrev_b32_e32 v94, 4, v11
	v_and_b32_e32 v11, 8, v29
	v_and_or_b32 v3, v12, 12, v3
	v_lshlrev_b32_e32 v6, 4, v6
	v_lshlrev_b32_e32 v8, 4, v8
	v_lshlrev_b32_e32 v58, 4, v10
	v_mad_u32_u24 v4, v119, s17, v4
	v_bitop3_b32 v12, v11, v3, 1 bitop3:0x36
	v_bitop3_b32 v13, v11, v3, 2 bitop3:0x36
	v_bitop3_b32 v14, v11, v3, 3 bitop3:0x36
	v_bitop3_b32 v15, v11, v3, 4 bitop3:0x36
	v_bitop3_b32 v16, v11, v3, 5 bitop3:0x36
	v_bitop3_b32 v17, v11, v3, 6 bitop3:0x36
	v_or_b32_e32 v7, v5, v6
	v_or_b32_e32 v9, v5, v8
	v_or_b32_e32 v10, v5, v58
	v_or_b32_e32 v5, v5, v94
	v_or_b32_e32 v6, v95, v6
	v_or_b32_e32 v60, v95, v8
	v_bitop3_b32 v8, v29, v3, 8 bitop3:0x6c
	v_bitop3_b32 v2, v11, v3, 7 bitop3:0x36
	v_lshl_or_b32 v112, v12, 4, v4
	v_lshl_or_b32 v126, v13, 4, v4
	v_lshl_or_b32 v130, v14, 4, v4
	v_lshl_or_b32 v134, v15, 4, v4
	v_lshl_or_b32 v138, v16, 4, v4
	v_lshl_or_b32 v142, v17, 4, v4
	v_lshl_or_b32 v103, v8, 4, v4
	v_lshl_or_b32 v148, v2, 4, v4
	ds_read_b128 v[22:25], v7
	ds_read_b128 v[18:21], v9
	ds_read_b128 v[14:17], v10
	ds_read_b128 v[10:13], v5
	ds_read_b128 v[6:9], v6
	ds_read_b128 v[2:5], v60
	ds_read_b128 v[108:111], v103
	ds_read_b128 v[112:115], v112
	ds_read_b128 v[126:129], v126
	ds_read_b128 v[130:133], v130
	ds_read_b128 v[134:137], v134
	ds_read_b128 v[138:141], v138
	ds_read_b128 v[142:145], v142
	v_bfe_u32 v103, v0, 6, 1
	s_movk_i32 s5, 0x2000
	s_waitcnt vmcnt(15) lgkmcnt(6)
	v_fma_mix_f32 v30, v30, v108, 0 op_sel_hi:[0,1,0]
	s_waitcnt vmcnt(14)
	v_fma_mix_f32 v30, v34, v110, v30 op_sel_hi:[0,1,0]
	v_fma_mix_f32 v30, v31, v108, v30 op_sel:[0,1,0] op_sel_hi:[0,1,0]
	v_fma_mix_f32 v30, v35, v110, v30 op_sel:[0,1,0] op_sel_hi:[0,1,0]
	v_fma_mix_f32 v30, v32, v109, v30 op_sel_hi:[0,1,0]
	v_fma_mix_f32 v30, v36, v111, v30 op_sel_hi:[0,1,0]
	v_fma_mix_f32 v30, v33, v109, v30 op_sel:[0,1,0] op_sel_hi:[0,1,0]
	v_fma_mix_f32 v30, v37, v111, v30 op_sel:[0,1,0] op_sel_hi:[0,1,0]
	s_waitcnt vmcnt(12) lgkmcnt(5)
	v_fma_mix_f32 v30, v42, v112, v30 op_sel_hi:[0,1,0]
	v_fma_mix_f32 v30, v38, v114, v30 op_sel_hi:[0,1,0]
	v_fma_mix_f32 v30, v43, v112, v30 op_sel:[0,1,0] op_sel_hi:[0,1,0]
	v_fma_mix_f32 v30, v39, v114, v30 op_sel:[0,1,0] op_sel_hi:[0,1,0]
	v_fma_mix_f32 v30, v44, v113, v30 op_sel_hi:[0,1,0]
	v_fma_mix_f32 v30, v40, v115, v30 op_sel_hi:[0,1,0]
	v_fma_mix_f32 v30, v45, v113, v30 op_sel:[0,1,0] op_sel_hi:[0,1,0]
	v_fma_mix_f32 v30, v41, v115, v30 op_sel:[0,1,0] op_sel_hi:[0,1,0]
	s_waitcnt vmcnt(10) lgkmcnt(4)
	v_fma_mix_f32 v30, v50, v126, v30 op_sel_hi:[0,1,0]
	v_fma_mix_f32 v30, v46, v128, v30 op_sel_hi:[0,1,0]
	v_fma_mix_f32 v30, v51, v126, v30 op_sel:[0,1,0] op_sel_hi:[0,1,0]
	v_fma_mix_f32 v30, v47, v128, v30 op_sel:[0,1,0] op_sel_hi:[0,1,0]
	v_fma_mix_f32 v30, v52, v127, v30 op_sel_hi:[0,1,0]
	v_fma_mix_f32 v30, v48, v129, v30 op_sel_hi:[0,1,0]
	v_fma_mix_f32 v30, v53, v127, v30 op_sel:[0,1,0] op_sel_hi:[0,1,0]
	v_fma_mix_f32 v30, v49, v129, v30 op_sel:[0,1,0] op_sel_hi:[0,1,0]
	s_waitcnt vmcnt(8) lgkmcnt(3)
	v_fma_mix_f32 v30, v62, v130, v30 op_sel_hi:[0,1,0]
	v_fma_mix_f32 v30, v54, v132, v30 op_sel_hi:[0,1,0]
	v_fma_mix_f32 v30, v63, v130, v30 op_sel:[0,1,0] op_sel_hi:[0,1,0]
	v_fma_mix_f32 v30, v55, v132, v30 op_sel:[0,1,0] op_sel_hi:[0,1,0]
	v_fma_mix_f32 v30, v64, v131, v30 op_sel_hi:[0,1,0]
	v_fma_mix_f32 v30, v56, v133, v30 op_sel_hi:[0,1,0]
	v_fma_mix_f32 v30, v65, v131, v30 op_sel:[0,1,0] op_sel_hi:[0,1,0]
	v_fma_mix_f32 v30, v57, v133, v30 op_sel:[0,1,0] op_sel_hi:[0,1,0]
	s_waitcnt vmcnt(6) lgkmcnt(2)
	v_fma_mix_f32 v30, v70, v134, v30 op_sel_hi:[0,1,0]
	v_fma_mix_f32 v30, v66, v136, v30 op_sel_hi:[0,1,0]
	v_fma_mix_f32 v30, v71, v134, v30 op_sel:[0,1,0] op_sel_hi:[0,1,0]
	v_fma_mix_f32 v30, v67, v136, v30 op_sel:[0,1,0] op_sel_hi:[0,1,0]
	v_fma_mix_f32 v30, v72, v135, v30 op_sel_hi:[0,1,0]
	v_fma_mix_f32 v30, v68, v137, v30 op_sel_hi:[0,1,0]
	v_fma_mix_f32 v30, v73, v135, v30 op_sel:[0,1,0] op_sel_hi:[0,1,0]
	v_fma_mix_f32 v30, v69, v137, v30 op_sel:[0,1,0] op_sel_hi:[0,1,0]
	s_waitcnt vmcnt(4) lgkmcnt(1)
	v_fma_mix_f32 v30, v78, v138, v30 op_sel_hi:[0,1,0]
	v_fma_mix_f32 v30, v74, v140, v30 op_sel_hi:[0,1,0]
	v_fma_mix_f32 v30, v79, v138, v30 op_sel:[0,1,0] op_sel_hi:[0,1,0]
	v_fma_mix_f32 v30, v75, v140, v30 op_sel:[0,1,0] op_sel_hi:[0,1,0]
	v_fma_mix_f32 v30, v80, v139, v30 op_sel_hi:[0,1,0]
	v_fma_mix_f32 v30, v76, v141, v30 op_sel_hi:[0,1,0]
	v_fma_mix_f32 v30, v81, v139, v30 op_sel:[0,1,0] op_sel_hi:[0,1,0]
	v_fma_mix_f32 v34, v77, v141, v30 op_sel:[0,1,0] op_sel_hi:[0,1,0]
	s_waitcnt vmcnt(2) lgkmcnt(0)
	v_fma_mix_f32 v34, v86, v142, v34 op_sel_hi:[0,1,0]
	v_fma_mix_f32 v34, v82, v144, v34 op_sel_hi:[0,1,0]
	v_fma_mix_f32 v34, v87, v142, v34 op_sel:[0,1,0] op_sel_hi:[0,1,0]
	ds_read_b128 v[30:33], v148
	v_fma_mix_f32 v34, v83, v144, v34 op_sel:[0,1,0] op_sel_hi:[0,1,0]
	v_fma_mix_f32 v34, v88, v143, v34 op_sel_hi:[0,1,0]
	v_fma_mix_f32 v34, v84, v145, v34 op_sel_hi:[0,1,0]
	v_fma_mix_f32 v34, v89, v143, v34 op_sel:[0,1,0] op_sel_hi:[0,1,0]
	v_fma_mix_f32 v34, v85, v145, v34 op_sel:[0,1,0] op_sel_hi:[0,1,0]
	s_waitcnt vmcnt(0) lgkmcnt(0)
	v_fma_mix_f32 v34, v104, v30, v34 op_sel_hi:[0,1,0]
	v_fma_mix_f32 v34, v90, v32, v34 op_sel_hi:[0,1,0]
	v_fma_mix_f32 v30, v105, v30, v34 op_sel:[0,1,0] op_sel_hi:[0,1,0]
	v_fma_mix_f32 v30, v91, v32, v30 op_sel:[0,1,0] op_sel_hi:[0,1,0]
	v_fma_mix_f32 v30, v106, v31, v30 op_sel_hi:[0,1,0]
	v_fma_mix_f32 v30, v92, v33, v30 op_sel_hi:[0,1,0]
	v_fma_mix_f32 v30, v107, v31, v30 op_sel:[0,1,0] op_sel_hi:[0,1,0]
	v_fma_mix_f32 v31, v93, v33, v30 op_sel:[0,1,0] op_sel_hi:[0,1,0]
	v_mbcnt_lo_u32_b32 v30, -1, 0
	v_mbcnt_hi_u32_b32 v32, -1, v30
	v_and_b32_e32 v33, 64, v32
	v_xor_b32_e32 v30, 16, v32
	v_add_u32_e32 v33, 64, v33
	v_cmp_lt_i32_e32 vcc, v30, v33
	v_mad_u32_u24 v44, v103, 48, v147
	v_lshlrev_b32_e32 v60, 8, v44
	v_cndmask_b32_e32 v30, v32, v30, vcc
	v_lshlrev_b32_e32 v30, 2, v30
	ds_bpermute_b32 v34, v30, v31
	v_lshlrev_b32_e32 v44, 2, v44
	v_or_b32_e32 v35, v95, v58
	v_lshlrev_b32_e32 v58, 14, v99
	v_and_b32_e32 v44, 12, v44
	s_waitcnt lgkmcnt(0)
	v_add_f32_e32 v130, v31, v34
	v_xor_b32_e32 v31, 32, v32
	v_cmp_lt_i32_e32 vcc, v31, v33
	v_or_b32_e32 v56, v44, v61
	v_bitop3_b32 v44, v101, v44, v61 bitop3:0x1e
	v_cndmask_b32_e32 v31, v32, v31, vcc
	v_lshl_add_u64 v[32:33], s[8:9], 0, v[58:59]
	v_lshlrev_b32_e32 v58, 4, v98
	v_or_b32_e32 v36, v95, v94
	v_lshl_add_u64 v[88:89], v[32:33], 0, v[58:59]
	v_lshl_or_b32 v57, v44, 4, v60
	ds_read_b128 v[40:43], v35
	ds_read_b128 v[106:109], v36
	s_load_dword s4, s[6:7], 0x0
	global_load_dwordx4 v[36:39], v[88:89], off
	global_load_dwordx4 v[32:35], v[88:89], off offset:1024
	ds_read_b128 v[44:47], v57
	v_bitop3_b32 v48, v101, v56, 4 bitop3:0x36
	v_lshl_or_b32 v62, v48, 4, v60
	ds_read_b128 v[48:51], v62
	v_bitop3_b32 v52, v101, v56, 8 bitop3:0x36
	v_lshl_or_b32 v63, v52, 4, v60
	ds_read_b128 v[52:55], v63
	s_waitcnt lgkmcnt(0)
	v_mfma_f32_16x16x32_f16 v[44:47], v[44:47], v[22:25], 0
	v_bitop3_b32 v64, v101, v56, 12 bitop3:0x36
	ds_read_b128 v[56:59], v57 offset:49152
	v_lshl_or_b32 v60, v64, 4, v60
	v_mfma_f32_16x16x32_f16 v[44:47], v[48:51], v[18:21], v[44:47]
	ds_read_b128 v[68:71], v60
	ds_read_b128 v[72:75], v62 offset:49152
	v_mad_u32_u24 v104, v103, 3, 1
	v_lshlrev_b32_e32 v132, 4, v104
	v_mfma_f32_16x16x32_f16 v[44:47], v[52:55], v[14:17], v[44:47]
	v_add_u32_e32 v52, v132, v147
	global_load_dwordx4 v[64:67], v[88:89], off offset:2048
	global_load_dwordx4 v[48:51], v[88:89], off offset:3072
	ds_read_b128 v[76:79], v63 offset:49152
	ds_read_b128 v[80:83], v60 offset:49152
	s_waitcnt lgkmcnt(3)
	v_mfma_f32_16x16x32_f16 v[44:47], v[68:71], v[10:13], v[44:47]
	v_lshlrev_b32_e32 v60, 8, v52
	v_lshlrev_b32_e32 v52, 2, v52
	v_and_b32_e32 v52, 12, v52
	v_mfma_f32_16x16x32_f16 v[44:47], v[56:59], v[6:9], v[44:47]
	v_or_b32_e32 v62, v52, v61
	v_bitop3_b32 v52, v101, v52, v61 bitop3:0x1e
	v_lshl_or_b32 v63, v52, 4, v60
	s_waitcnt lgkmcnt(2)
	v_mfma_f32_16x16x32_f16 v[44:47], v[72:75], v[2:5], v[44:47]
	ds_read_b128 v[52:55], v63
	v_bitop3_b32 v56, v101, v62, 4 bitop3:0x36
	v_lshl_or_b32 v84, v56, 4, v60
	s_waitcnt lgkmcnt(2)
	v_mfma_f32_16x16x32_f16 v[44:47], v[76:79], v[40:43], v[44:47]
	ds_read_b128 v[56:59], v84
	v_bitop3_b32 v68, v101, v62, 8 bitop3:0x36
	v_lshl_or_b32 v85, v68, 4, v60
	s_waitcnt lgkmcnt(2)
	v_mfma_f32_16x16x32_f16 v[110:113], v[80:83], v[106:109], v[44:47]
	ds_read_b128 v[68:71], v63 offset:49152
	v_bitop3_b32 v62, v101, v62, 12 bitop3:0x36
	v_lshl_or_b32 v60, v62, 4, v60
	ds_read_b128 v[44:47], v85
	s_waitcnt lgkmcnt(3)
	v_mfma_f32_16x16x32_f16 v[52:55], v[52:55], v[22:25], 0
	ds_read_b128 v[72:75], v60
	ds_read_b128 v[76:79], v84 offset:49152
	v_mad_u32_u24 v105, v103, 3, 2
	v_lshlrev_b32_e32 v133, 4, v105
	s_waitcnt lgkmcnt(4)
	v_mfma_f32_16x16x32_f16 v[52:55], v[56:59], v[18:21], v[52:55]
	ds_read_b128 v[56:59], v85 offset:49152
	v_add_co_u32_e32 v114, vcc, s15, v88
	s_waitcnt lgkmcnt(3)
	v_mfma_f32_16x16x32_f16 v[44:47], v[44:47], v[14:17], v[52:55]
	v_addc_co_u32_e32 v115, vcc, 0, v89, vcc
	v_lshlrev_b32_e32 v31, 2, v31
	s_waitcnt lgkmcnt(2)
	v_mfma_f32_16x16x32_f16 v[44:47], v[72:75], v[10:13], v[44:47]
	ds_read_b128 v[52:55], v60 offset:49152
	v_add_u32_e32 v60, v133, v147
	v_lshlrev_b32_e32 v72, 8, v60
	v_lshlrev_b32_e32 v60, 2, v60
	v_mfma_f32_16x16x32_f16 v[44:47], v[68:71], v[6:9], v[44:47]
	v_and_b32_e32 v60, 12, v60
	v_or_b32_e32 v68, v60, v61
	v_bitop3_b32 v60, v101, v60, v61 bitop3:0x1e
	v_lshl_or_b32 v69, v60, 4, v72
	s_waitcnt lgkmcnt(2)
	v_mfma_f32_16x16x32_f16 v[44:47], v[76:79], v[2:5], v[44:47]
	ds_read_b128 v[60:63], v69
	v_bitop3_b32 v70, v101, v68, 4 bitop3:0x36
	v_lshl_or_b32 v70, v70, 4, v72
	s_waitcnt lgkmcnt(2)
	v_mfma_f32_16x16x32_f16 v[44:47], v[56:59], v[40:43], v[44:47]
	ds_read_b128 v[56:59], v70
	v_bitop3_b32 v71, v101, v68, 8 bitop3:0x36
	v_lshl_or_b32 v71, v71, 4, v72
	s_waitcnt lgkmcnt(1)
	v_mfma_f32_16x16x32_f16 v[22:25], v[60:63], v[22:25], 0
	v_bitop3_b32 v60, v101, v68, 12 bitop3:0x36
	v_lshl_or_b32 v68, v60, 4, v72
	ds_bpermute_b32 v131, v31, v130
	v_mfma_f32_16x16x32_f16 v[126:129], v[52:55], v[106:109], v[44:47]
	s_nop 2
	ds_read_b128 v[44:47], v71
	ds_read_b128 v[52:55], v69 offset:49152
	ds_read_b128 v[60:63], v70 offset:49152
	s_waitcnt lgkmcnt(4)
	v_mfma_f32_16x16x32_f16 v[18:21], v[56:59], v[18:21], v[22:25]
	ds_read_b128 v[56:59], v71 offset:49152
	s_nop 1
	ds_read_b128 v[22:25], v68
	s_waitcnt lgkmcnt(4)
	v_mfma_f32_16x16x32_f16 v[14:17], v[44:47], v[14:17], v[18:21]
	v_add_co_u32_e32 v44, vcc, s5, v88
	s_movk_i32 s5, 0x3000
	s_nop 0
	ds_read_b128 v[18:21], v68 offset:49152
	s_waitcnt lgkmcnt(1)
	v_mfma_f32_16x16x32_f16 v[10:13], v[22:25], v[10:13], v[14:17]
	v_addc_co_u32_e32 v45, vcc, 0, v89, vcc
	global_load_dwordx4 v[84:87], v[114:115], off offset:1024
	global_load_dwordx4 v[80:83], v[114:115], off offset:2048
	global_load_dwordx4 v[92:95], v[44:45], off offset:-4096
	global_load_dwordx4 v[76:79], v[44:45], off
	v_mfma_f32_16x16x32_f16 v[6:9], v[52:55], v[6:9], v[10:13]
	global_load_dwordx4 v[72:75], v[44:45], off offset:1024
	global_load_dwordx4 v[68:71], v[44:45], off offset:2048
	global_load_dwordx4 v[52:55], v[44:45], off offset:3072
	v_mov_b32_e32 v13, 0xff61b1e6
	v_mfma_f32_16x16x32_f16 v[2:5], v[60:63], v[2:5], v[6:9]
	s_nop 2
	v_add_co_u32_e32 v6, vcc, s5, v88
	v_mfma_f32_16x16x32_f16 v[2:5], v[56:59], v[40:43], v[2:5]
	s_nop 0
	v_addc_co_u32_e32 v7, vcc, 0, v89, vcc
	global_load_dwordx4 v[88:91], v[114:115], off offset:3072
	global_load_dwordx4 v[60:63], v[6:7], off
	global_load_dwordx4 v[56:59], v[6:7], off offset:1024
	global_load_dwordx4 v[44:47], v[6:7], off offset:2048
	global_load_dwordx4 v[40:43], v[6:7], off offset:3072
	s_waitcnt lgkmcnt(0)
	v_mfma_f32_16x16x32_f16 v[16:19], v[18:21], v[106:109], v[2:5]
	v_add_f32_e32 v6, v130, v131
	s_mov_b32 s5, 0xff61b1e6
	s_nop 0
	v_or_b32_e32 v3, s14, v146
	v_mov_b32_e32 v4, 0x7df
	v_med3_u32 v3, v3, 32, v4
	v_or_b32_e32 v4, v97, v102
	v_sub_u32_e32 v3, v4, v3
	v_add_f32_e32 v2, s4, v6
	v_add_u32_e32 v3, 32, v3
	v_mad_u32_u24 v4, v103, 48, v3
	s_movk_i32 s4, 0x41
	v_add_f32_e32 v5, v2, v110
	v_mul_f32_e32 v5, 0x3db8aa3b, v5
	v_cmp_gt_u32_e32 vcc, s4, v4
	v_add_u32_e32 v6, 1, v4
	v_add_f32_e32 v7, v2, v111
	v_cndmask_b32_e32 v5, v13, v5, vcc
	v_mul_f32_e32 v7, 0x3db8aa3b, v7
	v_cmp_gt_u32_e32 vcc, s4, v6
	v_add_u32_e32 v8, 2, v4
	v_add_f32_e32 v9, v2, v112
	v_cndmask_b32_e32 v6, v13, v7, vcc
	v_mul_f32_e32 v9, 0x3db8aa3b, v9
	v_cmp_gt_u32_e32 vcc, s4, v8
	v_add_u32_e32 v4, 3, v4
	v_max3_f32 v7, v5, s5, v6
	v_cndmask_b32_e32 v8, v13, v9, vcc
	v_add_f32_e32 v9, v2, v113
	v_mul_f32_e32 v9, 0x3db8aa3b, v9
	v_cmp_gt_u32_e32 vcc, s4, v4
	v_add_u32_e32 v11, v3, v132
	v_add_f32_e32 v12, v2, v127
	v_cndmask_b32_e32 v10, v13, v9, vcc
	v_max3_f32 v4, v7, v8, v10
	v_add_f32_e32 v7, v2, v126
	v_mul_f32_e32 v7, 0x3db8aa3b, v7
	v_cmp_gt_u32_e32 vcc, s4, v11
	v_add_u32_e32 v9, 1, v11
	v_mul_f32_e32 v12, 0x3db8aa3b, v12
	v_cndmask_b32_e32 v7, v13, v7, vcc
	v_cmp_gt_u32_e32 vcc, s4, v9
	v_add_f32_e32 v14, v2, v128
	v_mul_f32_e32 v14, 0x3db8aa3b, v14
	v_cndmask_b32_e32 v9, v13, v12, vcc
	v_add_u32_e32 v12, 2, v11
	v_cmp_gt_u32_e32 vcc, s4, v12
	v_add_u32_e32 v11, 3, v11
	v_add_u32_e32 v3, v3, v133
	v_cndmask_b32_e32 v12, v13, v14, vcc
	v_add_f32_e32 v14, v2, v129
	v_mul_f32_e32 v14, 0x3db8aa3b, v14
	v_cmp_gt_u32_e32 vcc, s4, v11
	v_add_f32_e32 v11, v2, v16
	v_mul_f32_e32 v11, 0x3db8aa3b, v11
	v_cndmask_b32_e32 v15, v13, v14, vcc
	v_cmp_gt_u32_e32 vcc, s4, v3
	v_add_u32_e32 v14, 1, v3
	v_add_f32_e32 v16, v2, v17
	v_cndmask_b32_e32 v11, v13, v11, vcc
	v_mul_f32_e32 v16, 0x3db8aa3b, v16
	v_cmp_gt_u32_e32 vcc, s4, v14
	v_add_f32_e32 v17, v2, v18
	v_max3_f32 v4, v4, v7, v9
	v_cndmask_b32_e32 v14, v13, v16, vcc
	v_add_u32_e32 v16, 2, v3
	v_mul_f32_e32 v17, 0x3db8aa3b, v17
	v_cmp_gt_u32_e32 vcc, s4, v16
	v_add_u32_e32 v3, 3, v3
	v_add_f32_e32 v2, v2, v19
	v_max3_f32 v4, v4, v12, v15
	v_cndmask_b32_e32 v16, v13, v17, vcc
	v_mul_f32_e32 v2, 0x3db8aa3b, v2
	v_cmp_gt_u32_e32 vcc, s4, v3
	v_max3_f32 v4, v4, v11, v14
	v_lshlrev_b32_e32 v126, 5, v99
	v_cndmask_b32_e32 v17, v13, v2, vcc
	v_max3_f32 v2, v4, v16, v17
	ds_bpermute_b32 v3, v30, v2
	v_lshlrev_b32_e32 v127, 2, v119
	v_lshrrev_b32_e32 v4, 7, v0
	v_cmp_gt_u32_e32 vcc, 16, v98
	s_waitcnt lgkmcnt(0)
	v_max_f32_e32 v3, v3, v3
	v_max_f32_e32 v2, v2, v3
	ds_bpermute_b32 v3, v31, v2
	s_waitcnt lgkmcnt(0)
	v_max_f32_e32 v3, v3, v3
	v_max_f32_e32 v13, v2, v3
	v_and_b32_e32 v2, 0x180, v0
	v_or_b32_e32 v2, 0x23400, v2
	v_lshlrev_b32_e32 v3, 2, v100
	s_and_saveexec_b64 s[4:5], vcc
	v_lshlrev_b32_e32 v18, 6, v103
	v_add3_u32 v18, v2, v18, v3
	ds_write_b32 v18, v13
	s_or_b64 exec, exec, s[4:5]
	v_lshlrev_b32_e32 v18, 4, v103
	v_bitop3_b32 v19, v18, 16, v100 bitop3:0x36
	v_lshl_add_u32 v2, v19, 2, v2
	s_waitcnt lgkmcnt(0)
	s_barrier
	ds_read_b32 v19, v2
	v_max_f32_e32 v13, v13, v13
	v_mul_u32_u24_e32 v20, 0xd00, v4
	s_load_dwordx2 s[0:1], s[0:1], 0x30
	v_or_b32_e32 v2, 1, v124
	s_waitcnt lgkmcnt(0)
	v_max_f32_e32 v19, v19, v19
	v_max_f32_e32 v19, v13, v19
	v_sub_f32_e32 v5, v5, v19
	v_exp_f32_e32 v5, v5
	v_sub_f32_e32 v6, v6, v19
	v_exp_f32_e32 v6, v6
	v_sub_f32_e32 v8, v8, v19
	v_mul_u32_u24_e32 v13, 0xd0, v100
	v_exp_f32_e32 v8, v8
	v_sub_f32_e32 v10, v10, v19
	v_add3_u32 v20, v13, v20, v29
	v_exp_f32_e32 v10, v10
	v_or_b32_e32 v22, 0x20000, v20
	v_add_f32_e32 v20, 0, v5
	v_add_f32_e32 v20, v20, v6
	v_add_f32_e32 v20, v20, v8
	v_add_f32_e32 v23, v20, v10
	v_cvt_pk_f16_f32 v21, v8, v10
	v_cvt_pk_f16_f32 v20, v5, v6
	v_mad_u32_u24 v5, v103, s16, v22
	ds_write_b64 v5, v[20:21]
	v_sub_f32_e32 v5, v7, v19
	v_exp_f32_e32 v5, v5
	v_sub_f32_e32 v6, v9, v19
	v_exp_f32_e32 v6, v6
	v_sub_f32_e32 v7, v12, v19
	v_exp_f32_e32 v7, v7
	v_sub_f32_e32 v8, v15, v19
	v_exp_f32_e32 v8, v8
	v_sub_f32_e32 v10, v11, v19
	v_add_f32_e32 v9, v23, v5
	v_exp_f32_e32 v10, v10
	v_sub_f32_e32 v11, v14, v19
	v_add_f32_e32 v9, v9, v6
	v_exp_f32_e32 v11, v11
	v_sub_f32_e32 v12, v16, v19
	v_add_f32_e32 v9, v9, v7
	v_exp_f32_e32 v12, v12
	v_sub_f32_e32 v14, v17, v19
	v_add_f32_e32 v9, v9, v8
	v_exp_f32_e32 v14, v14
	v_add_f32_e32 v9, v9, v10
	v_add_f32_e32 v9, v9, v11
	v_add_f32_e32 v9, v9, v12
	v_add_f32_e32 v9, v9, v14
	ds_bpermute_b32 v15, v30, v9
	v_cvt_pk_f16_f32 v7, v7, v8
	v_cvt_pk_f16_f32 v6, v5, v6
	v_lshl_add_u32 v5, v104, 5, v22
	ds_write_b64 v5, v[6:7]
	s_waitcnt lgkmcnt(1)
	v_add_f32_e32 v5, v9, v15
	ds_bpermute_b32 v6, v31, v5
	s_movk_i32 s7, 0xd00
	s_mov_b32 s6, 0x20000
	v_cvt_pk_f16_f32 v9, v12, v14
	v_cvt_pk_f16_f32 v8, v10, v11
	v_lshl_add_u32 v7, v105, 5, v22
	ds_write_b64 v7, v[8:9]
	s_and_saveexec_b64 s[4:5], vcc
	s_cbranch_execz .LBB1_4
	v_lshlrev_b32_e32 v4, 5, v4
	v_or_b32_e32 v7, v18, v100
	v_lshlrev_b32_e32 v4, 2, v4
	v_lshlrev_b32_e32 v7, 2, v7
	s_mov_b32 s8, 0x23600
	v_add3_u32 v4, v7, v4, s8
	s_waitcnt lgkmcnt(1)
	v_add_f32_e32 v5, v5, v6
	ds_write_b32 v4, v5

	.amdhsa_kernel _Z7na_mainPKDF16_PKhS0_PKfS4_S4_S4_Pf
		.amdhsa_group_segment_fixed_size 161792
		.amdhsa_private_segment_fixed_size 0
		.amdhsa_kernarg_size 64
		.amdhsa_user_sgpr_count 2
		.amdhsa_user_sgpr_dispatch_ptr 0
		.amdhsa_user_sgpr_queue_ptr 0
		.amdhsa_user_sgpr_kernarg_segment_ptr 1
		.amdhsa_user_sgpr_dispatch_id 0
		.amdhsa_user_sgpr_kernarg_preload_length 0
		.amdhsa_user_sgpr_kernarg_preload_offset 0
		.amdhsa_user_sgpr_private_segment_size 0
		.amdhsa_uses_dynamic_stack 0
		.amdhsa_enable_private_segment 0
		.amdhsa_system_sgpr_workgroup_id_x 1
		.amdhsa_system_sgpr_workgroup_id_y 0
		.amdhsa_system_sgpr_workgroup_id_z 0
		.amdhsa_system_sgpr_workgroup_info 0
		.amdhsa_system_vgpr_workitem_id 0
		.amdhsa_next_free_vgpr 192
		.amdhsa_next_free_sgpr 96
		.amdhsa_accum_offset 192
		.amdhsa_reserve_vcc 1
		.amdhsa_float_round_mode_32 0
		.amdhsa_float_round_mode_16_64 0
		.amdhsa_float_denorm_mode_32 3
		.amdhsa_float_denorm_mode_16_64 3
		.amdhsa_dx10_clamp 1
		.amdhsa_ieee_mode 1
		.amdhsa_fp16_overflow 0
		.amdhsa_tg_split 0
		.amdhsa_exception_fp_ieee_invalid_op 0
		.amdhsa_exception_fp_denorm_src 0
		.amdhsa_exception_fp_ieee_div_zero 0
		.amdhsa_exception_fp_ieee_overflow 0
		.amdhsa_exception_fp_ieee_underflow 0
		.amdhsa_exception_fp_ieee_inexact 0
		.amdhsa_exception_int_div_zero 0
	.end_amdhsa_kernel

amdhsa.kernels:
  - .agpr_count:     16
    .args:
      - .actual_access:  read_only
        .address_space:  global
        .offset:         0
        .size:           8
        .value_kind:     global_buffer
      - .actual_access:  read_only
        .address_space:  global
        .offset:         8
        .size:           8
        .value_kind:     global_buffer
      - .actual_access:  read_only
        .address_space:  global
        .offset:         16
        .size:           8
        .value_kind:     global_buffer
      - .actual_access:  read_only
        .address_space:  global
        .offset:         24
        .size:           8
        .value_kind:     global_buffer
      - .actual_access:  read_only
        .address_space:  global
        .offset:         32
        .size:           8
        .value_kind:     global_buffer
      - .actual_access:  read_only
        .address_space:  global
        .offset:         40
        .size:           8
        .value_kind:     global_buffer
      - .actual_access:  write_only
        .address_space:  global
        .offset:         48
        .size:           8
        .value_kind:     global_buffer
      - .actual_access:  write_only
        .address_space:  global
        .offset:         56
        .size:           8
        .value_kind:     global_buffer
      - .actual_access:  write_only
        .address_space:  global
        .offset:         64
        .size:           8
        .value_kind:     global_buffer
      - .actual_access:  write_only
        .address_space:  global
        .offset:         72
        .size:           8
        .value_kind:     global_buffer
      - .actual_access:  write_only
        .address_space:  global
        .offset:         80
        .size:           8
        .value_kind:     global_buffer
      - .actual_access:  write_only
        .address_space:  global
        .offset:         88
        .size:           8
        .value_kind:     global_buffer
    .group_segment_fixed_size: 16384
    .kernarg_segment_align: 8
    .kernarg_segment_size: 96
    .language:       OpenCL C
    .language_version:
      - 2
      - 0
    .max_flat_workgroup_size: 256
    .name:           _Z7na_prepPKfS0_S0_S0_S0_S0_PDF16_PhS1_PfS3_S3_
    .private_segment_fixed_size: 0
    .sgpr_count:     23
    .sgpr_spill_count: 0
    .symbol:         _Z7na_prepPKfS0_S0_S0_S0_S0_PDF16_PhS1_PfS3_S3_.kd
    .uniform_work_group_size: 1
    .uses_dynamic_stack: false
    .vgpr_count:     116
    .vgpr_spill_count: 0
    .wavefront_size: 64
  - .agpr_count:     0
    .args:
      - .address_space:  global
        .offset:         0
        .size:           8
        .value_kind:     global_buffer
      - .actual_access:  read_only
        .address_space:  global
        .offset:         8
        .size:           8
        .value_kind:     global_buffer
      - .actual_access:  read_only
        .address_space:  global
        .offset:         16
        .size:           8
        .value_kind:     global_buffer
      - .actual_access:  read_only
        .address_space:  global
        .offset:         24
        .size:           8
        .value_kind:     global_buffer
      - .actual_access:  read_only
        .address_space:  global
        .offset:         32
        .size:           8
        .value_kind:     global_buffer
      - .actual_access:  read_only
        .address_space:  global
        .offset:         40
        .size:           8
        .value_kind:     global_buffer
      - .actual_access:  read_only
        .address_space:  global
        .offset:         48
        .size:           8
        .value_kind:     global_buffer
      - .actual_access:  write_only
        .address_space:  global
        .offset:         56
        .size:           8
        .value_kind:     global_buffer
    .group_segment_fixed_size: 161792
    .kernarg_segment_align: 8
    .kernarg_segment_size: 64
    .language:       OpenCL C
    .language_version:
      - 2
      - 0
    .max_flat_workgroup_size: 512
    .name:           _Z7na_mainPKDF16_PKhS0_PKfS4_S4_S4_Pf
    .private_segment_fixed_size: 0
    .sgpr_count:     24
    .sgpr_spill_count: 0
    .symbol:         _Z7na_mainPKDF16_PKhS0_PKfS4_S4_S4_Pf.kd
    .uniform_work_group_size: 1
    .uses_dynamic_stack: false
    .vgpr_count:     192
    .vgpr_spill_count: 0
    .wavefront_size: 64
